# v18: v17 + removed now-redundant MFMA hazard pads in DSA/DIFF hot paths
# baseline (speedup 1.0000x reference)
; template <int MODE, int DQK, int DV>
; __device__ __forceinline__ void attn_pass(LAS unsigned char* lds, const Tens& T, size_t rowbase, int q0, f32x16 (&o)[DV / 32], float& l_out, const int wave, QPre* qp = nullptr) {
;     ...
;             psum = 0.f;
; #pragma unroll
;             for (int rg = 0; rg < 16; ++rg) { const float e0 = __builtin_amdgcn_exp2f(p[0][rg]), e1 = __builtin_amdgcn_exp2f(p[1][rg]); p[0][rg] = e0; p[1][rg] = e1; psum += e0; psum += e1; }
;             if (!POSTHOC || redo) break;
;             if (__builtin_expect(!__any(!(psum <= BIG)), 1)) break;
;             redo = true;
.LBB0_1655:
	v_exp_f32_e32 v122, v32
	v_exp_f32_e32 v32, v48
	v_exp_f32_e32 v48, v33
	v_exp_f32_e32 v33, v49
	v_add_f32_e32 v49, 0, v122
	v_add_f32_e32 v49, v32, v49
	v_add_f32_e32 v123, v48, v49
	v_exp_f32_e32 v49, v34
	v_exp_f32_e32 v34, v50
	v_add_f32_e32 v123, v33, v123
	v_exp_f32_e32 v50, v35
	v_add_f32_e32 v35, v49, v123
	v_add_f32_e32 v123, v34, v35
	v_exp_f32_e32 v35, v51
	v_exp_f32_e32 v51, v36
	v_exp_f32_e32 v36, v52
	v_add_f32_e32 v123, v50, v123
	v_add_f32_e32 v123, v35, v123
	v_exp_f32_e32 v52, v37
	v_add_f32_e32 v37, v51, v123
	v_add_f32_e32 v123, v36, v37
	v_exp_f32_e32 v37, v53
	v_exp_f32_e32 v53, v38
	v_exp_f32_e32 v38, v54
	v_add_f32_e32 v123, v52, v123
	v_add_f32_e32 v123, v37, v123
	v_exp_f32_e32 v54, v39
	v_add_f32_e32 v39, v53, v123
	v_add_f32_e32 v123, v38, v39
	v_exp_f32_e32 v39, v55
	v_exp_f32_e32 v55, v40
	v_exp_f32_e32 v40, v56
	v_add_f32_e32 v123, v54, v123
	v_add_f32_e32 v123, v39, v123
	v_exp_f32_e32 v56, v41
	v_add_f32_e32 v41, v55, v123
	v_add_f32_e32 v123, v40, v41
	v_exp_f32_e32 v41, v57
	v_exp_f32_e32 v57, v42
	v_exp_f32_e32 v42, v58
	v_add_f32_e32 v123, v56, v123
	v_add_f32_e32 v123, v41, v123
	v_exp_f32_e32 v58, v43
	v_add_f32_e32 v43, v57, v123
	v_add_f32_e32 v123, v42, v43
	v_exp_f32_e32 v43, v59
	v_exp_f32_e32 v59, v44
	v_exp_f32_e32 v44, v60
	v_add_f32_e32 v123, v58, v123
	v_add_f32_e32 v123, v43, v123
	v_exp_f32_e32 v60, v45
	v_add_f32_e32 v45, v59, v123
	v_add_f32_e32 v123, v44, v45
	v_exp_f32_e32 v45, v61
	v_exp_f32_e32 v61, v46
	v_exp_f32_e32 v46, v62
	v_add_f32_e32 v123, v60, v123
	v_add_f32_e32 v123, v45, v123
	v_exp_f32_e32 v62, v47
	v_add_f32_e32 v47, v61, v123
	v_add_f32_e32 v123, v46, v47
	v_exp_f32_e32 v47, v63
	v_add_f32_e32 v63, v62, v123
	s_andn2_b64 vcc, exec, s[36:37]
	v_add_f32_e32 v63, v47, v63
	s_cbranch_vccnz .LBB0_1657
	v_cmp_nge_f32_e32 vcc, s80, v63
	s_cbranch_vccnz .LBB0_1690

; template <int MODE, int DQK, int DV>
; __device__ __forceinline__ void attn_pass(LAS unsigned char* lds, const Tens& T, size_t rowbase, int q0, f32x16 (&o)[DV / 32], float& l_out, const int wave, QPre* qp = nullptr) {
;     ...
;             psum = 0.f;
; #pragma unroll
;             for (int rg = 0; rg < 16; ++rg) { const float e0 = __builtin_amdgcn_exp2f(p[0][rg]), e1 = __builtin_amdgcn_exp2f(p[1][rg]); p[0][rg] = e0; p[1][rg] = e1; psum += e0; psum += e1; }
;             if (!POSTHOC || redo) break;
;             if (__builtin_expect(!__any(!(psum <= BIG)), 1)) break;
.LBB0_1660:
	v_exp_f32_e32 v122, v32
	v_exp_f32_e32 v32, v48
	v_exp_f32_e32 v48, v33
	v_exp_f32_e32 v33, v49
	v_add_f32_e32 v49, 0, v122
	v_add_f32_e32 v49, v32, v49
	v_add_f32_e32 v49, v48, v49
	v_add_f32_e32 v123, v33, v49
	v_exp_f32_e32 v49, v34
	v_exp_f32_e32 v34, v50
	v_exp_f32_e32 v50, v35
	v_exp_f32_e32 v35, v51
	v_add_f32_e32 v51, v49, v123
	v_add_f32_e32 v51, v34, v51
	v_add_f32_e32 v51, v50, v51
	v_add_f32_e32 v123, v35, v51
	v_exp_f32_e32 v51, v36
	v_exp_f32_e32 v36, v52
	v_exp_f32_e32 v52, v37
	v_exp_f32_e32 v37, v53
	v_add_f32_e32 v53, v51, v123
	v_add_f32_e32 v53, v36, v53
	v_add_f32_e32 v53, v52, v53
	v_add_f32_e32 v123, v37, v53
	v_exp_f32_e32 v53, v38
	v_exp_f32_e32 v38, v54
	v_exp_f32_e32 v54, v39
	v_exp_f32_e32 v39, v55
	v_add_f32_e32 v55, v53, v123
	v_add_f32_e32 v55, v38, v55
	v_add_f32_e32 v55, v54, v55
	v_add_f32_e32 v123, v39, v55
	v_exp_f32_e32 v55, v40
	v_exp_f32_e32 v40, v56
	v_exp_f32_e32 v56, v41
	v_exp_f32_e32 v41, v57
	v_add_f32_e32 v57, v55, v123
	v_add_f32_e32 v57, v40, v57
	v_add_f32_e32 v57, v56, v57
	v_add_f32_e32 v123, v41, v57
	v_exp_f32_e32 v57, v42
	v_exp_f32_e32 v42, v58
	v_exp_f32_e32 v58, v43
	v_exp_f32_e32 v43, v59
	v_add_f32_e32 v59, v57, v123
	v_add_f32_e32 v59, v42, v59
	v_add_f32_e32 v59, v58, v59
	v_add_f32_e32 v123, v43, v59
	v_exp_f32_e32 v59, v44
	v_exp_f32_e32 v44, v60
	v_exp_f32_e32 v60, v45
	v_exp_f32_e32 v45, v61
	v_add_f32_e32 v61, v59, v123
	v_add_f32_e32 v61, v44, v61
	v_add_f32_e32 v61, v60, v61
	v_add_f32_e32 v123, v45, v61
	v_exp_f32_e32 v61, v46
	v_exp_f32_e32 v46, v62
	v_exp_f32_e32 v62, v47
	v_exp_f32_e32 v47, v63
	v_add_f32_e32 v63, v61, v123
	v_add_f32_e32 v63, v46, v63
	v_add_f32_e32 v63, v62, v63
	v_add_f32_e32 v63, v47, v63
	v_cmp_nge_f32_e32 vcc, s80, v63
	s_cbranch_vccnz .LBB0_1687

; template <int MODE, int DQK, int DV>
; __device__ __forceinline__ void attn_pass(LAS unsigned char* lds, const Tens& T, size_t rowbase, int q0, f32x16 (&o)[DV / 32], float& l_out, const int wave, QPre* qp = nullptr) {
;     ...
;             psum = 0.f;
; #pragma unroll
;             for (int rg = 0; rg < 16; ++rg) { const float e0 = __builtin_amdgcn_exp2f(p[0][rg]), e1 = __builtin_amdgcn_exp2f(p[1][rg]); p[0][rg] = e0; p[1][rg] = e1; psum += e0; psum += e1; }
;             if (!POSTHOC || redo) break;
;             if (__builtin_expect(!__any(!(psum <= BIG)), 1)) break;
.LBB0_1668:
	v_exp_f32_e32 v121, v32
	v_exp_f32_e32 v32, v48
	v_exp_f32_e32 v48, v33
	v_exp_f32_e32 v33, v49
	v_add_f32_e32 v49, 0, v121
	v_add_f32_e32 v49, v32, v49
	v_add_f32_e32 v49, v48, v49
	v_add_f32_e32 v122, v33, v49
	v_exp_f32_e32 v49, v34
	v_exp_f32_e32 v34, v50
	v_exp_f32_e32 v50, v35
	v_exp_f32_e32 v35, v51
	v_add_f32_e32 v51, v49, v122
	v_add_f32_e32 v51, v34, v51
	v_add_f32_e32 v51, v50, v51
	v_add_f32_e32 v122, v35, v51
	v_exp_f32_e32 v51, v36
	v_exp_f32_e32 v36, v52
	v_exp_f32_e32 v52, v37
	v_exp_f32_e32 v37, v53
	v_add_f32_e32 v53, v51, v122
	v_add_f32_e32 v53, v36, v53
	v_add_f32_e32 v53, v52, v53
	v_add_f32_e32 v122, v37, v53
	v_exp_f32_e32 v53, v38
	v_exp_f32_e32 v38, v54
	v_exp_f32_e32 v54, v39
	v_exp_f32_e32 v39, v55
	v_add_f32_e32 v55, v53, v122
	v_add_f32_e32 v55, v38, v55
	v_add_f32_e32 v55, v54, v55
	v_add_f32_e32 v122, v39, v55
	v_exp_f32_e32 v55, v40
	v_exp_f32_e32 v40, v56
	v_exp_f32_e32 v56, v41
	v_exp_f32_e32 v41, v57
	v_add_f32_e32 v57, v55, v122
	v_add_f32_e32 v57, v40, v57
	v_add_f32_e32 v57, v56, v57
	v_add_f32_e32 v122, v41, v57
	v_exp_f32_e32 v57, v42
	v_exp_f32_e32 v42, v58
	v_exp_f32_e32 v58, v43
	v_exp_f32_e32 v43, v59
	v_add_f32_e32 v59, v57, v122
	v_add_f32_e32 v59, v42, v59
	v_add_f32_e32 v59, v58, v59
	v_add_f32_e32 v122, v43, v59
	v_exp_f32_e32 v59, v44
	v_exp_f32_e32 v44, v60
	v_exp_f32_e32 v60, v45
	v_exp_f32_e32 v45, v61
	v_add_f32_e32 v61, v59, v122
	v_add_f32_e32 v61, v44, v61
	v_add_f32_e32 v61, v60, v61
	v_add_f32_e32 v122, v45, v61
	v_exp_f32_e32 v61, v46
	v_exp_f32_e32 v46, v62
	v_exp_f32_e32 v62, v47
	v_exp_f32_e32 v47, v63
	v_add_f32_e32 v63, v61, v122
	v_add_f32_e32 v63, v46, v63
	v_add_f32_e32 v63, v62, v63
	v_add_f32_e32 v63, v47, v63
	v_cmp_nge_f32_e32 vcc, s80, v63
	s_cbranch_vccnz .LBB0_1693

; template <int MODE, int DQK, int DV>
; __device__ __forceinline__ void attn_pass(LAS unsigned char* lds, const Tens& T, size_t rowbase, int q0, f32x16 (&o)[DV / 32], float& l_out, const int wave, QPre* qp = nullptr) {
;     ...
;             psum = 0.f;
; #pragma unroll
;             for (int rg = 0; rg < 16; ++rg) { const float e0 = __builtin_amdgcn_exp2f(p[0][rg]), e1 = __builtin_amdgcn_exp2f(p[1][rg]); p[0][rg] = e0; p[1][rg] = e1; psum += e0; psum += e1; }
;             if (!POSTHOC || redo) break;
;             if (__builtin_expect(!__any(!(psum <= BIG)), 1)) break;
;             redo = true;
;             }
.LBB0_2451:
	v_exp_f32_e32 v13, v96
	v_exp_f32_e32 v3, v112
	v_exp_f32_e32 v15, v97
	v_exp_f32_e32 v4, v113
	v_add_f32_e32 v2, 0, v13
	v_exp_f32_e32 v97, v98
	v_add_f32_e32 v2, v3, v2
	v_exp_f32_e32 v5, v114
	v_add_f32_e32 v2, v15, v2
	v_exp_f32_e32 v99, v99
	v_add_f32_e32 v2, v4, v2
	v_exp_f32_e32 v6, v115
	v_add_f32_e32 v2, v97, v2
	v_exp_f32_e32 v112, v100
	v_add_f32_e32 v2, v5, v2
	v_exp_f32_e32 v7, v116
	v_add_f32_e32 v2, v99, v2
	v_exp_f32_e32 v113, v101
	v_add_f32_e32 v2, v6, v2
	v_exp_f32_e32 v8, v117
	v_add_f32_e32 v2, v112, v2
	v_exp_f32_e32 v114, v102
	v_add_f32_e32 v2, v7, v2
	v_exp_f32_e32 v9, v118
	v_add_f32_e32 v2, v113, v2
	v_exp_f32_e32 v115, v103
	v_add_f32_e32 v2, v8, v2
	v_exp_f32_e32 v11, v119
	v_add_f32_e32 v2, v114, v2
	v_exp_f32_e32 v103, v104
	v_add_f32_e32 v2, v9, v2
	v_exp_f32_e32 v10, v120
	v_add_f32_e32 v2, v115, v2
	v_exp_f32_e32 v104, v105
	v_add_f32_e32 v2, v11, v2
	v_exp_f32_e32 v12, v121
	v_add_f32_e32 v2, v103, v2
	v_exp_f32_e32 v105, v106
	v_add_f32_e32 v2, v10, v2
	v_exp_f32_e32 v14, v122
	v_add_f32_e32 v2, v104, v2
	v_exp_f32_e32 v106, v107
	v_add_f32_e32 v2, v12, v2
	v_exp_f32_e32 v96, v123
	v_add_f32_e32 v2, v105, v2
	v_exp_f32_e32 v107, v108
	v_add_f32_e32 v2, v14, v2
	v_exp_f32_e32 v98, v124
	v_add_f32_e32 v2, v106, v2
	v_exp_f32_e32 v108, v109
	v_add_f32_e32 v2, v96, v2
	v_exp_f32_e32 v100, v125
	v_add_f32_e32 v2, v107, v2
	v_exp_f32_e32 v109, v110
	v_add_f32_e32 v2, v98, v2
	v_exp_f32_e32 v101, v126
	v_add_f32_e32 v2, v108, v2
	v_exp_f32_e32 v110, v111
	v_add_f32_e32 v2, v100, v2
	v_exp_f32_e32 v102, v127
	v_add_f32_e32 v2, v109, v2
	v_add_f32_e32 v2, v101, v2
	s_xor_b64 s[2:3], s[72:73], -1
	v_add_f32_e32 v2, v110, v2
	v_add_f32_e32 v2, v102, v2
	s_mov_b64 s[72:73], -1
	s_andn2_b64 vcc, exec, s[2:3]
	s_mov_b64 s[2:3], -1
	s_cbranch_vccnz .LBB0_2446
	v_cmp_nge_f32_e32 vcc, s88, v2
	s_cmp_eq_u64 vcc, 0
	s_cselect_b64 s[2:3], -1, 0
	s_branch .LBB0_2446
